# expert-weight conversion split: GLA workgroups convert 16 items in scan, last 8 items moved to the out-projection phase tail on workgroups 128-255 (idle third GEMM round); last layer keeps all 24 in s
# speedup vs baseline: 1.0054x; 1.0054x over previous
; __device__ __forceinline__ void cvb_load(CArgs& a, int l, int bit, int w, int lane, CvbRegs& r) {
;     const int kbb = bit & 7, nb = (bit >> 3) & 3, m = bit >> 5, e = m / 3, which = m - 3 * e;
;     const float* W = a.in[which == 0 ? I_WG : (which == 1 ? I_WU : I_WD)] + ((size_t)(l * NEXP + e)) * 1024 * 1024 + (size_t)(128 * kbb + 16 * w) * 1024 + 256 * nb + 4 * lane;
; #pragma unroll
;     for (int j = 0; j < 16; ++j) r.t[j] = *(const f32x4*)(W + (size_t)j * 1024);
; }
; __device__ __forceinline__ void ph_scan(CArgs& a, int l, LAS unsigned char* lds, int bid, int nblk, unsigned long long& tacc) {
;     ...
;         if (nblk == 256) { const int per = bid < 128 ? 8 : 16, first = bid < 128 ? bid * 8 : 1024 + (bid - 128) * 16;
;             CvbRegs r0, r1;
;             cvb_load(a, l, first, w, lane, r0);
; #pragma unroll 1
;             for (int it = first; it < first + per; it += 2) {
;                 cvb_load(a, l, it + 1, w, lane, r1);
;                 cvb_store(a, it, w, lane, r0, lds);
;                 cvb_load(a, l, min(it + 2, first + per - 1), w, lane, r0);
;                 cvb_store(a, it + 1, w, lane, r1, lds + 36864); } }
.LBB0_2662:
	s_andn2_b64 vcc, exec, s[2:3]
	s_cbranch_vccnz .LBB0_2697
	v_readlane_b32 s0, v251, 7
	s_cmpk_lt_i32 s0, 0x80
	s_cbranch_scc1 .LBB0_2697
	s_lshl_b32 s10, s0, 4
	s_addk_i32 s10, 0xf800
	s_add_i32 s6, s10, 16
.Lcvt_setup:
	v_and_b32_e32 v160, 63, v0
	v_writelane_b32 v250, s10, 1
	s_lshl_b32 s0, s10, 7
	v_writelane_b32 v250, s0, 2
	s_lshl_b32 s4, s10, 5
	v_writelane_b32 v252, s4, 27
	v_writelane_b32 v252, s6, 28
	s_add_i32 s5, s6, -1
	v_writelane_b32 v252, s5, 29
	s_and_b32 s4, s4, 0x300
	s_lshl_b32 s0, s4, 2
	v_writelane_b32 v252, s0, 56
	s_ashr_i32 s1, s10, 5
	s_mul_hi_i32 s4, s1, 0x55555556
	s_lshr_b32 s5, s4, 31
	s_add_i32 s4, s4, s5
	v_writelane_b32 v252, s4, 26
	s_mul_i32 s4, s4, -3
	s_add_i32 s4, s4, s1
	s_cmp_eq_u32 s4, 1
	s_cselect_b32 s1, 33, 35
	s_cmp_lg_u32 s4, 0
	s_cselect_b32 s1, s1, 31
	s_lshl_b32 s0, s1, 3
	v_writelane_b32 v252, s0, 55
	s_nop 1
	v_readlane_b32 s0, v252, 55
	s_load_dwordx2 s[2:3], s[30:31], s0 offset:0x0
	s_lshl_b32 s0, s84, 5
	v_readlane_b32 s1, v252, 26
	s_add_i32 s4, s0, s1
	s_ashr_i32 s5, s4, 31
	s_lshl_b64 s[4:5], s[4:5], 22
	s_waitcnt lgkmcnt(0)
	s_add_u32 s1, s2, s4
	v_readlane_b32 s2, v249, 3
	s_addc_u32 s6, s3, s5
	s_lshl_b32 s2, s2, 4
	s_ashr_i32 s3, s2, 31
	s_lshl_b64 s[4:5], s[2:3], 12
	s_add_u32 s1, s1, s4
	s_addc_u32 s3, s6, s5
	v_readlane_b32 s4, v252, 56
	s_add_u32 s4, s1, s4
	s_addc_u32 s5, s3, 0
	v_lshlrev_b32_e32 v34, 4, v160
	s_waitcnt vmcnt(0)
	v_lshl_add_u64 v[64:65], s[4:5], 0, v[34:35]
	s_movk_i32 s1, 0x2000
	s_waitcnt vmcnt(0)
	v_add_co_u32_e32 v6, vcc, s1, v64
	s_movk_i32 s1, 0x4000
	s_nop 0
	v_addc_co_u32_e32 v7, vcc, 0, v65, vcc
	global_load_dwordx4 v[2:5], v34, s[4:5]
	global_load_dwordx4 v[10:13], v[6:7], off offset:-4096
	global_load_dwordx4 v[14:17], v[6:7], off
	v_add_co_u32_e32 v6, vcc, s1, v64
	s_movk_i32 s1, 0x6000
	s_nop 0
	v_addc_co_u32_e32 v7, vcc, 0, v65, vcc
	global_load_dwordx4 v[30:33], v[6:7], off offset:-4096
	global_load_dwordx4 v[18:21], v[6:7], off
	v_add_co_u32_e32 v6, vcc, s1, v64
	s_mov_b32 s1, 0x8000
	s_nop 0
	v_addc_co_u32_e32 v7, vcc, 0, v65, vcc
	global_load_dwordx4 v[40:43], v[6:7], off offset:-4096
	global_load_dwordx4 v[44:47], v[6:7], off
	v_add_co_u32_e32 v6, vcc, s1, v64
	s_mov_b32 s1, 0xa000
	s_nop 0
	v_addc_co_u32_e32 v7, vcc, 0, v65, vcc
	v_add_co_u32_e32 v26, vcc, s1, v64
	s_mov_b32 s1, 0xc000
	s_nop 0
	v_addc_co_u32_e32 v27, vcc, 0, v65, vcc
	v_add_co_u32_e32 v36, vcc, s1, v64
	s_mov_b32 s1, 0xe000
	s_nop 0
	v_addc_co_u32_e32 v37, vcc, 0, v65, vcc
	v_add_co_u32_e32 v56, vcc, s1, v64
	s_mov_b32 s1, 0xf000
	s_nop 0
	v_addc_co_u32_e32 v57, vcc, 0, v65, vcc
	v_add_co_u32_e32 v64, vcc, s1, v64
	global_load_dwordx4 v[60:63], v[6:7], off offset:-4096
	s_nop 0
	global_load_dwordx4 v[6:9], v[6:7], off
	v_addc_co_u32_e32 v65, vcc, 0, v65, vcc
	global_load_dwordx4 v[22:25], v[26:27], off offset:-4096
	s_nop 0
	global_load_dwordx4 v[26:29], v[26:27], off
	s_nop 0
	global_load_dwordx4 v[48:51], v[36:37], off offset:-4096
	s_nop 0
	global_load_dwordx4 v[36:39], v[36:37], off
	s_nop 0
	global_load_dwordx4 v[52:55], v[56:57], off offset:-4096
	s_nop 0
	global_load_dwordx4 v[56:59], v[56:57], off
	s_load_dwordx2 s[6:7], s[30:31], 0x140
	global_load_dwordx4 v[64:67], v[64:65], off
	v_readlane_b32 s1, v249, 2
	s_andn2_b32 s1, s1, 63
	v_and_b32_e32 v132, 0x70, v34
	v_or_b32_e32 v70, s1, v160
	v_add_u32_e32 v34, 0x200, v70
	s_add_i32 s8, s2, 0
	v_ashrrev_i32_e32 v135, 3, v34
	v_add_u32_e32 v34, 0x400, v70
	s_waitcnt lgkmcnt(0)
	s_add_u32 s4, s6, 0x4800000
	v_ashrrev_i32_e32 v137, 3, v34
	v_add_u32_e32 v34, 0x600, v70
	s_addc_u32 s5, s7, 0
	v_ashrrev_i32_e32 v1, 3, v70
	v_ashrrev_i32_e32 v139, 3, v34
	v_lshlrev_b32_e32 v68, 2, v160
	v_mul_u32_u24_e32 v69, 0x240, v160
	v_add_u32_e32 v71, 0, v132
	s_add_u32 s1, s6, 0xc800000
	v_mul_lo_u32 v72, v1, s75
	v_mul_lo_u32 v73, v135, s75
	v_mul_lo_u32 v74, v137, s75
	v_mul_lo_u32 v70, v139, s75
	v_mov_b32_e32 v133, v35
	s_addc_u32 s3, s7, 0
	v_and_b32_e32 v134, 0x7f, v1
	v_and_b32_e32 v136, 0x7f, v135
	v_and_b32_e32 v138, 0x7f, v137
	v_and_b32_e32 v140, 0x7f, v139
	v_lshlrev_b32_e32 v34, 2, v68
	v_add_u32_e32 v141, s8, v69
	v_add_u32_e32 v150, v71, v72
	v_add_u32_e32 v151, v71, v73
	v_add_u32_e32 v152, v71, v74
	v_add_u32_e32 v153, v71, v70
	v_readlane_b32 s8, v250, 2
	v_readlane_b32 s9, v252, 27
	v_readlane_b32 s10, v250, 1
	s_branch .LBB0_2665

; __device__ __forceinline__ void ph_scan(CArgs& a, int l, LAS unsigned char* lds, int bid, int nblk, unsigned long long& tacc) {
;     ...
;         if (nblk == 256) { const int per = bid < 128 ? 8 : 16, first = bid < 128 ? bid * 8 : 1024 + (bid - 128) * 16;
;             CvbRegs r0, r1;
;             cvb_load(a, l, first, w, lane, r0);
; #pragma unroll 1
;             for (int it = first; it < first + per; it += 2) {
;                 cvb_load(a, l, it + 1, w, lane, r1);
;                 cvb_store(a, it, w, lane, r0, lds);
;                 cvb_load(a, l, min(it + 2, first + per - 1), w, lane, r0);
;                 cvb_store(a, it + 1, w, lane, r1, lds + 36864); } }
.Lcvt_done:
	v_readlane_b32 s0, v250, 1
	s_nop 3
	s_cmpk_lt_i32 s0, 0x800
	s_cbranch_scc0 .Lcvt_done2
	s_cmp_lg_u32 s84, 3
	s_cbranch_scc1 .LBB0_2697
	v_readlane_b32 s0, v251, 7
	s_nop 3
	s_lshl_b32 s10, s0, 3
	s_addk_i32 s10, 0x400
	s_add_i32 s6, s10, 8
	s_branch .Lcvt_setup
.Lcvt_done2:
	s_cmp_lg_u32 s84, 3
	s_cbranch_scc1 .Lcvt_ret

; __device__ __forceinline__ unsigned xb_add(unsigned* p, unsigned v) { return __hip_atomic_fetch_add(p, v, __ATOMIC_RELAXED, __HIP_MEMORY_SCOPE_AGENT); }
; __device__ __forceinline__ CArgs* kargs() { CArgs* p = (CArgs*)__builtin_amdgcn_kernarg_segment_ptr(); asm volatile("" : "+s"(p)); return p; }
; #define PB_BEG(ty) do { if (PROBE_PH == (ty)) tbeg = __builtin_amdgcn_s_memrealtime(); } while (0)
; #define PB_END(ty) do { if (PROBE_PH == (ty)) tacc += __builtin_amdgcn_s_memrealtime() - tbeg; } while (0)
; #define SEAM(k) do { if (IN(k) && IN((k) + 1)) xcd_barrier(bar); } while (0)
; __device__ __forceinline__ void xcd_barrier(const XcdBarrier& b) {
;     asm volatile("s_waitcnt vmcnt(0)" ::: "memory");
;     __syncthreads();
;     if (threadIdx.x == 0) {
;         unsigned* bar = b.bar;
;         __builtin_amdgcn_s_waitcnt(0);
;         unsigned nloc = b.st[0], nx = b.st[1];
;         if (nloc == 0u) { xcd_barrier_complete(bar, b.x, nloc, nx); b.st[0] = nloc; b.st[1] = nx; }
;         const unsigned old = xb_add(&bar[XB_XSUB(b.x)], 1u);
; __global__ void __launch_bounds__(512, 2) trunk_fwd(Args a_unused) {
;     ...
;         if (IN(p0 + 4)) {
;             CArgs& a = *kargs();
;             const int r0 = lastl ? NTOK_C : 0;
;             pg8::DenseSched S; S.init((const bf16*)(a.ws + WS_WOUT) + (size_t)l * 1024 * 1024, 1024, NTOK - r0, 1024, nblk, bid, r0);
;             pg8::EpiBf16 E{(bf16*)(a.ws + WS_TMP), 1024, r0};
;             pg8::gemm_phase<pg8::EpiBf16, pg8::DenseSched, true>(lds, (const char*)(a.ws + WS_YMIX), 1024, S, E);
;         }
;         SEAM(p0 + 4); PB_END(6); PB_BEG(7);
.LBB0_2840:
	s_cmp_eq_u32 s84, 3
	s_cbranch_scc1 .Lcvt_skip
	s_cmpk_lt_i32 s64, 0x80
	s_cbranch_scc1 .Lcvt_skip
	v_and_b32_e32 v160, 63, v0
	v_readfirstlane_b32 s2, v0
	v_readlane_b32 s30, v251, 2
	v_readlane_b32 s31, v251, 3
	s_nop 3
	v_writelane_b32 v249, s2, 2
	s_ashr_i32 s0, s2, 6
	v_writelane_b32 v249, s30, 0
	v_writelane_b32 v249, s31, 1
	v_writelane_b32 v249, s0, 3
	s_lshl_b32 s10, s64, 3
	s_addk_i32 s10, 0x400
	s_add_i32 s6, s10, 8
	s_branch .Lcvt_setup
.Lcvt_ret:
.Lcvt_skip:
	v_readlane_b32 s0, v250, 57
	s_add_i32 s0, s0, 7
	s_cmp_ge_i32 s0, s83
	s_cbranch_scc1 .LBB0_2890
	s_waitcnt vmcnt(0)
	s_waitcnt vmcnt(0)
	s_barrier
	s_mov_b64 s[2:3], exec
	v_readlane_b32 s4, v250, 15
	v_readlane_b32 s5, v250, 16
	s_and_b64 s[4:5], s[2:3], s[4:5]
	s_mov_b64 exec, s[4:5]
	s_cbranch_execz .LBB0_2889
	v_readlane_b32 s1, v251, 13
	s_waitcnt vmcnt(0) expcnt(0) lgkmcnt(0)
	s_nop 0
	v_mov_b32_e32 v1, s1
	ds_read_b32 v3, v1
	ds_read_b32 v2, v1 offset:4
	s_waitcnt lgkmcnt(1)
	v_cmp_ne_u32_e32 vcc, 0, v3
	s_cbranch_vccnz .LBB0_2857
	v_readlane_b32 s6, v251, 0
	v_readlane_b32 s7, v251, 1
	s_load_dwordx2 s[4:5], s[6:7], 0x4
	s_mov_b32 s8, 1
	s_waitcnt lgkmcnt(0)
	s_mul_i32 s1, s4, s68
	s_mul_i32 s1, s1, s5
	s_branch .LBB0_2845
